# baseline (speedup 1.0000x reference)
_Z8dog_mainPKfS0_S0_S0_S0_S0_S0_Pf:
	s_load_dwordx8 s[12:19], s[0:1], 0x0
	s_load_dwordx8 s[20:27], s[0:1], 0x20
	s_and_b32 s3, s2, 7
	s_lshl_b32 s3, s3, 5
	s_lshr_b32 s4, s2, 3
	s_add_i32 s4, s3, s4
	s_and_b32 s6, s4, 3
	s_lshr_b32 s7, s4, 2
	s_mov_b32 s5, 0
	s_lshl_b64 s[8:9], s[4:5], 18
	v_and_b32_e32 v1, 63, v0
	v_lshrrev_b32_e32 v2, 6, v0
	v_and_b32_e32 v3, 31, v0
	v_lshl_or_b32 v4, v2, 5, v3
	v_lshlrev_b32_e32 v5, 2, v4
	v_lshlrev_b32_e32 v6, 4, v1
	v_lshl_or_b32 v6, v2, 12, v6
	v_readfirstlane_b32 s28, v2
	s_waitcnt lgkmcnt(0)
	global_load_dword v20, v5, s[18:19]
	global_load_dword v21, v5, s[20:21]
	global_load_dword v22, v5, s[22:23]
	global_load_dword v23, v5, s[24:25]
	global_load_dword v24, v5, s[14:15]
	global_load_dword v25, v5, s[16:17]
	s_add_u32 s12, s12, s8
	s_addc_u32 s13, s13, s9
	s_cmp_ge_u32 s28, 4
	s_cbranch_scc1 .Lsetup
.Lloads:
	global_load_dwordx4 v[128:131], v6, s[12:13] offset:0 nt
	global_load_dwordx4 v[132:135], v6, s[12:13] offset:1024 nt
	global_load_dwordx4 v[136:139], v6, s[12:13] offset:2048 nt
	global_load_dwordx4 v[140:143], v6, s[12:13] offset:3072 nt
	v_add_u32_e32 v6, 0x8000, v6
	global_load_dwordx4 v[144:147], v6, s[12:13] offset:0 nt
	global_load_dwordx4 v[148:151], v6, s[12:13] offset:1024 nt
	global_load_dwordx4 v[152:155], v6, s[12:13] offset:2048 nt
	global_load_dwordx4 v[156:159], v6, s[12:13] offset:3072 nt
	v_add_u32_e32 v6, 0x8000, v6
	global_load_dwordx4 v[160:163], v6, s[12:13] offset:0 nt
	global_load_dwordx4 v[164:167], v6, s[12:13] offset:1024 nt
	global_load_dwordx4 v[168:171], v6, s[12:13] offset:2048 nt
	global_load_dwordx4 v[172:175], v6, s[12:13] offset:3072 nt
	v_add_u32_e32 v6, 0x8000, v6
	global_load_dwordx4 v[176:179], v6, s[12:13] offset:0 nt
	global_load_dwordx4 v[180:183], v6, s[12:13] offset:1024 nt
	global_load_dwordx4 v[184:187], v6, s[12:13] offset:2048 nt
	global_load_dwordx4 v[188:191], v6, s[12:13] offset:3072 nt
	v_add_u32_e32 v6, 0x8000, v6
	global_load_dwordx4 v[192:195], v6, s[12:13] offset:0 nt
	global_load_dwordx4 v[196:199], v6, s[12:13] offset:1024 nt
	global_load_dwordx4 v[200:203], v6, s[12:13] offset:2048 nt
	global_load_dwordx4 v[204:207], v6, s[12:13] offset:3072 nt
	v_add_u32_e32 v6, 0x8000, v6
	global_load_dwordx4 v[208:211], v6, s[12:13] offset:0 nt
	global_load_dwordx4 v[212:215], v6, s[12:13] offset:1024 nt
	global_load_dwordx4 v[216:219], v6, s[12:13] offset:2048 nt
	global_load_dwordx4 v[220:223], v6, s[12:13] offset:3072 nt
	v_add_u32_e32 v6, 0x8000, v6
	global_load_dwordx4 v[224:227], v6, s[12:13] offset:0 nt
	global_load_dwordx4 v[228:231], v6, s[12:13] offset:1024 nt
	global_load_dwordx4 v[232:235], v6, s[12:13] offset:2048 nt
	global_load_dwordx4 v[236:239], v6, s[12:13] offset:3072 nt
	v_add_u32_e32 v6, 0x8000, v6
	global_load_dwordx4 v[240:243], v6, s[12:13] offset:0 nt
	global_load_dwordx4 v[244:247], v6, s[12:13] offset:1024 nt
	global_load_dwordx4 v[248:251], v6, s[12:13] offset:2048 nt
	global_load_dwordx4 v[252:255], v6, s[12:13] offset:3072 nt
	s_cmp_ge_u32 s28, 4
	s_cbranch_scc1 .Lconsume
.Lsetup:
	v_bfe_u32 v7, v0, 5, 1
	v_and_b32_e32 v16, 1, v0
	v_cmp_eq_u32_e64 s[30:31], 0, v16
	v_and_b32_e32 v17, 2, v0
	v_cmp_eq_u32_e64 s[32:33], 0, v17
	v_and_b32_e32 v16, 3, v0
	v_lshrrev_b32_e32 v17, 2, v1
	v_lshlrev_b32_e32 v16, 5, v16
	v_lshl_add_u32 v16, v17, 1, v16
	v_lshrrev_b32_e32 v17, 1, v2
	s_movk_i32 s10, 0x110
	v_mad_u32_u24 v16, v17, s10, v16
	v_and_b32_e32 v17, 1, v2
	v_lshl_add_u32 v14, v17, 7, v16
	v_lshlrev_b32_e32 v17, 4, v7
	v_mad_u32_u24 v15, v3, s10, v17
	s_lshl_b32 s11, s6, 5
	v_lshl_add_u32 v18, v7, 2, s11
	v_cvt_f32_u32_e32 v18, v18
	v_lshlrev_b32_e32 v19, 3, v7
	v_cvt_f32_u32_e32 v19, v19
	s_cmp_ge_u32 s28, 4
	s_cbranch_scc1 .Lparams_b
	s_waitcnt vmcnt(32)
	s_branch .Ltables
.Lparams_b:
	s_waitcnt vmcnt(0)
.Ltables:
	v_add_f32_e32 v26, v20, v21
	v_rcp_f32_e32 v27, v20
	v_rcp_f32_e32 v28, v26
	v_sub_f32_e32 v12, v19, v22
	v_sub_f32_e32 v13, v18, v23
	v_fma_f32 v29, -v20, v27, 1.0
	v_fma_f32 v30, -v26, v28, 1.0
	v_fma_f32 v27, v29, v27, v27
	v_fma_f32 v28, v30, v28, v28
	v_mul_f32_e32 v8, 0xbf38aa3b, v27
	v_mul_f32_e32 v9, 0xbf38aa3b, v28
	v_mul_f32_e32 v29, v24, v27
	v_mul_f32_e32 v30, v25, v28
	v_mul_f32_e32 v10, 0x3e22f983, v29
	v_mul_f32_e32 v11, 0x3e22f983, v30
	v_mul_f32_e32 v16, v12, v12
	v_add_f32_e32 v17, 0x3f800000, v12
	v_add_f32_e32 v18, 0x40000000, v12
	v_add_f32_e32 v19, 0x40400000, v12
	v_mul_f32_e32 v17, v17, v17
	v_mul_f32_e32 v18, v18, v18
	v_mul_f32_e32 v19, v19, v19
	v_mul_f32_e32 v20, v8, v16
	v_mul_f32_e32 v24, v9, v16
	v_mul_f32_e32 v21, v8, v17
	v_mul_f32_e32 v25, v9, v17
	v_mul_f32_e32 v22, v8, v18
	v_mul_f32_e32 v26, v9, v18
	v_mul_f32_e32 v23, v8, v19
	v_mul_f32_e32 v27, v9, v19
	v_exp_f32_e32 v20, v20
	v_exp_f32_e32 v21, v21
	v_exp_f32_e32 v22, v22
	v_exp_f32_e32 v23, v23
	v_exp_f32_e32 v24, v24
	v_exp_f32_e32 v25, v25
	v_exp_f32_e32 v26, v26
	v_exp_f32_e32 v27, v27
	v_cvt_pk_f16_f32 v32, v20, v21
	v_cvt_pk_f16_f32 v33, v22, v23
	v_cvt_pk_f16_f32 v64, v24, v25
	v_cvt_pk_f16_f32 v65, v26, v27
	v_add_f32_e32 v16, 0x40800000, v12
	v_add_f32_e32 v17, 0x40a00000, v12
	v_add_f32_e32 v18, 0x40c00000, v12
	v_add_f32_e32 v19, 0x40e00000, v12
	v_mul_f32_e32 v16, v16, v16
	v_mul_f32_e32 v17, v17, v17
	v_mul_f32_e32 v18, v18, v18
	v_mul_f32_e32 v19, v19, v19
	v_mul_f32_e32 v20, v8, v16
	v_mul_f32_e32 v24, v9, v16
	v_mul_f32_e32 v21, v8, v17
	v_mul_f32_e32 v25, v9, v17
	v_mul_f32_e32 v22, v8, v18
	v_mul_f32_e32 v26, v9, v18
	v_mul_f32_e32 v23, v8, v19
	v_mul_f32_e32 v27, v9, v19
	v_exp_f32_e32 v20, v20
	v_exp_f32_e32 v21, v21
	v_exp_f32_e32 v22, v22
	v_exp_f32_e32 v23, v23
	v_exp_f32_e32 v24, v24
	v_exp_f32_e32 v25, v25
	v_exp_f32_e32 v26, v26
	v_exp_f32_e32 v27, v27
	v_cvt_pk_f16_f32 v34, v20, v21
	v_cvt_pk_f16_f32 v35, v22, v23
	v_cvt_pk_f16_f32 v66, v24, v25
	v_cvt_pk_f16_f32 v67, v26, v27
	v_add_f32_e32 v16, 0x41800000, v12
	v_add_f32_e32 v17, 0x41880000, v12
	v_add_f32_e32 v18, 0x41900000, v12
	v_add_f32_e32 v19, 0x41980000, v12
	v_mul_f32_e32 v16, v16, v16
	v_mul_f32_e32 v17, v17, v17
	v_mul_f32_e32 v18, v18, v18
	v_mul_f32_e32 v19, v19, v19
	v_mul_f32_e32 v20, v8, v16
	v_mul_f32_e32 v24, v9, v16
	v_mul_f32_e32 v21, v8, v17
	v_mul_f32_e32 v25, v9, v17
	v_mul_f32_e32 v22, v8, v18
	v_mul_f32_e32 v26, v9, v18
	v_mul_f32_e32 v23, v8, v19
	v_mul_f32_e32 v27, v9, v19
	v_exp_f32_e32 v20, v20
	v_exp_f32_e32 v21, v21
	v_exp_f32_e32 v22, v22
	v_exp_f32_e32 v23, v23
	v_exp_f32_e32 v24, v24
	v_exp_f32_e32 v25, v25
	v_exp_f32_e32 v26, v26
	v_exp_f32_e32 v27, v27
	v_cvt_pk_f16_f32 v36, v20, v21
	v_cvt_pk_f16_f32 v37, v22, v23
	v_cvt_pk_f16_f32 v68, v24, v25
	v_cvt_pk_f16_f32 v69, v26, v27
	v_add_f32_e32 v16, 0x41a00000, v12
	v_add_f32_e32 v17, 0x41a80000, v12
	v_add_f32_e32 v18, 0x41b00000, v12
	v_add_f32_e32 v19, 0x41b80000, v12
	v_mul_f32_e32 v16, v16, v16
	v_mul_f32_e32 v17, v17, v17
	v_mul_f32_e32 v18, v18, v18
	v_mul_f32_e32 v19, v19, v19
	v_mul_f32_e32 v20, v8, v16
	v_mul_f32_e32 v24, v9, v16
	v_mul_f32_e32 v21, v8, v17
	v_mul_f32_e32 v25, v9, v17
	v_mul_f32_e32 v22, v8, v18
	v_mul_f32_e32 v26, v9, v18
	v_mul_f32_e32 v23, v8, v19
	v_mul_f32_e32 v27, v9, v19
	v_exp_f32_e32 v20, v20
	v_exp_f32_e32 v21, v21
	v_exp_f32_e32 v22, v22
	v_exp_f32_e32 v23, v23
	v_exp_f32_e32 v24, v24
	v_exp_f32_e32 v25, v25
	v_exp_f32_e32 v26, v26
	v_exp_f32_e32 v27, v27
	v_cvt_pk_f16_f32 v38, v20, v21
	v_cvt_pk_f16_f32 v39, v22, v23
	v_cvt_pk_f16_f32 v70, v24, v25
	v_cvt_pk_f16_f32 v71, v26, v27
	v_add_f32_e32 v16, 0x42000000, v12
	v_add_f32_e32 v17, 0x42040000, v12
	v_add_f32_e32 v18, 0x42080000, v12
	v_add_f32_e32 v19, 0x420c0000, v12
	v_mul_f32_e32 v16, v16, v16
	v_mul_f32_e32 v17, v17, v17
	v_mul_f32_e32 v18, v18, v18
	v_mul_f32_e32 v19, v19, v19
	v_mul_f32_e32 v20, v8, v16
	v_mul_f32_e32 v24, v9, v16
	v_mul_f32_e32 v21, v8, v17
	v_mul_f32_e32 v25, v9, v17
	v_mul_f32_e32 v22, v8, v18
	v_mul_f32_e32 v26, v9, v18
	v_mul_f32_e32 v23, v8, v19
	v_mul_f32_e32 v27, v9, v19
	v_exp_f32_e32 v20, v20
	v_exp_f32_e32 v21, v21
	v_exp_f32_e32 v22, v22
	v_exp_f32_e32 v23, v23
	v_exp_f32_e32 v24, v24
	v_exp_f32_e32 v25, v25
	v_exp_f32_e32 v26, v26
	v_exp_f32_e32 v27, v27
	v_cvt_pk_f16_f32 v40, v20, v21
	v_cvt_pk_f16_f32 v41, v22, v23
	v_cvt_pk_f16_f32 v72, v24, v25
	v_cvt_pk_f16_f32 v73, v26, v27
	v_add_f32_e32 v16, 0x42100000, v12
	v_add_f32_e32 v17, 0x42140000, v12
	v_add_f32_e32 v18, 0x42180000, v12
	v_add_f32_e32 v19, 0x421c0000, v12
	v_mul_f32_e32 v16, v16, v16
	v_mul_f32_e32 v17, v17, v17
	v_mul_f32_e32 v18, v18, v18
	v_mul_f32_e32 v19, v19, v19
	v_mul_f32_e32 v20, v8, v16
	v_mul_f32_e32 v24, v9, v16
	v_mul_f32_e32 v21, v8, v17
	v_mul_f32_e32 v25, v9, v17
	v_mul_f32_e32 v22, v8, v18
	v_mul_f32_e32 v26, v9, v18
	v_mul_f32_e32 v23, v8, v19
	v_mul_f32_e32 v27, v9, v19
	v_exp_f32_e32 v20, v20
	v_exp_f32_e32 v21, v21
	v_exp_f32_e32 v22, v22
	v_exp_f32_e32 v23, v23
	v_exp_f32_e32 v24, v24
	v_exp_f32_e32 v25, v25
	v_exp_f32_e32 v26, v26
	v_exp_f32_e32 v27, v27
	v_cvt_pk_f16_f32 v42, v20, v21
	v_cvt_pk_f16_f32 v43, v22, v23
	v_cvt_pk_f16_f32 v74, v24, v25
	v_cvt_pk_f16_f32 v75, v26, v27
	v_add_f32_e32 v16, 0x42400000, v12
	v_add_f32_e32 v17, 0x42440000, v12
	v_add_f32_e32 v18, 0x42480000, v12
	v_add_f32_e32 v19, 0x424c0000, v12
	v_mul_f32_e32 v16, v16, v16
	v_mul_f32_e32 v17, v17, v17
	v_mul_f32_e32 v18, v18, v18
	v_mul_f32_e32 v19, v19, v19
	v_mul_f32_e32 v20, v8, v16
	v_mul_f32_e32 v24, v9, v16
	v_mul_f32_e32 v21, v8, v17
	v_mul_f32_e32 v25, v9, v17
	v_mul_f32_e32 v22, v8, v18
	v_mul_f32_e32 v26, v9, v18
	v_mul_f32_e32 v23, v8, v19
	v_mul_f32_e32 v27, v9, v19
	v_exp_f32_e32 v20, v20
	v_exp_f32_e32 v21, v21
	v_exp_f32_e32 v22, v22
	v_exp_f32_e32 v23, v23
	v_exp_f32_e32 v24, v24
	v_exp_f32_e32 v25, v25
	v_exp_f32_e32 v26, v26
	v_exp_f32_e32 v27, v27
	v_cvt_pk_f16_f32 v44, v20, v21
	v_cvt_pk_f16_f32 v45, v22, v23
	v_cvt_pk_f16_f32 v76, v24, v25
	v_cvt_pk_f16_f32 v77, v26, v27
	v_add_f32_e32 v16, 0x42500000, v12
	v_add_f32_e32 v17, 0x42540000, v12
	v_add_f32_e32 v18, 0x42580000, v12
	v_add_f32_e32 v19, 0x425c0000, v12
	v_mul_f32_e32 v16, v16, v16
	v_mul_f32_e32 v17, v17, v17
	v_mul_f32_e32 v18, v18, v18
	v_mul_f32_e32 v19, v19, v19
	v_mul_f32_e32 v20, v8, v16
	v_mul_f32_e32 v24, v9, v16
	v_mul_f32_e32 v21, v8, v17
	v_mul_f32_e32 v25, v9, v17
	v_mul_f32_e32 v22, v8, v18
	v_mul_f32_e32 v26, v9, v18
	v_mul_f32_e32 v23, v8, v19
	v_mul_f32_e32 v27, v9, v19
	v_exp_f32_e32 v20, v20
	v_exp_f32_e32 v21, v21
	v_exp_f32_e32 v22, v22
	v_exp_f32_e32 v23, v23
	v_exp_f32_e32 v24, v24
	v_exp_f32_e32 v25, v25
	v_exp_f32_e32 v26, v26
	v_exp_f32_e32 v27, v27
	v_cvt_pk_f16_f32 v46, v20, v21
	v_cvt_pk_f16_f32 v47, v22, v23
	v_cvt_pk_f16_f32 v78, v24, v25
	v_cvt_pk_f16_f32 v79, v26, v27
	v_add_f32_e32 v16, 0x42800000, v12
	v_add_f32_e32 v17, 0x42820000, v12
	v_add_f32_e32 v18, 0x42840000, v12
	v_add_f32_e32 v19, 0x42860000, v12
	v_mul_f32_e32 v16, v16, v16
	v_mul_f32_e32 v17, v17, v17
	v_mul_f32_e32 v18, v18, v18
	v_mul_f32_e32 v19, v19, v19
	v_mul_f32_e32 v20, v8, v16
	v_mul_f32_e32 v24, v9, v16
	v_mul_f32_e32 v21, v8, v17
	v_mul_f32_e32 v25, v9, v17
	v_mul_f32_e32 v22, v8, v18
	v_mul_f32_e32 v26, v9, v18
	v_mul_f32_e32 v23, v8, v19
	v_mul_f32_e32 v27, v9, v19
	v_exp_f32_e32 v20, v20
	v_exp_f32_e32 v21, v21
	v_exp_f32_e32 v22, v22
	v_exp_f32_e32 v23, v23
	v_exp_f32_e32 v24, v24
	v_exp_f32_e32 v25, v25
	v_exp_f32_e32 v26, v26
	v_exp_f32_e32 v27, v27
	v_cvt_pk_f16_f32 v48, v20, v21
	v_cvt_pk_f16_f32 v49, v22, v23
	v_cvt_pk_f16_f32 v80, v24, v25
	v_cvt_pk_f16_f32 v81, v26, v27
	v_add_f32_e32 v16, 0x42880000, v12
	v_add_f32_e32 v17, 0x428a0000, v12
	v_add_f32_e32 v18, 0x428c0000, v12
	v_add_f32_e32 v19, 0x428e0000, v12
	v_mul_f32_e32 v16, v16, v16
	v_mul_f32_e32 v17, v17, v17
	v_mul_f32_e32 v18, v18, v18
	v_mul_f32_e32 v19, v19, v19
	v_mul_f32_e32 v20, v8, v16
	v_mul_f32_e32 v24, v9, v16
	v_mul_f32_e32 v21, v8, v17
	v_mul_f32_e32 v25, v9, v17
	v_mul_f32_e32 v22, v8, v18
	v_mul_f32_e32 v26, v9, v18
	v_mul_f32_e32 v23, v8, v19
	v_mul_f32_e32 v27, v9, v19
	v_exp_f32_e32 v20, v20
	v_exp_f32_e32 v21, v21
	v_exp_f32_e32 v22, v22
	v_exp_f32_e32 v23, v23
	v_exp_f32_e32 v24, v24
	v_exp_f32_e32 v25, v25
	v_exp_f32_e32 v26, v26
	v_exp_f32_e32 v27, v27
	v_cvt_pk_f16_f32 v50, v20, v21
	v_cvt_pk_f16_f32 v51, v22, v23
	v_cvt_pk_f16_f32 v82, v24, v25
	v_cvt_pk_f16_f32 v83, v26, v27
	v_add_f32_e32 v16, 0x42a00000, v12
	v_add_f32_e32 v17, 0x42a20000, v12
	v_add_f32_e32 v18, 0x42a40000, v12
	v_add_f32_e32 v19, 0x42a60000, v12
	v_mul_f32_e32 v16, v16, v16
	v_mul_f32_e32 v17, v17, v17
	v_mul_f32_e32 v18, v18, v18
	v_mul_f32_e32 v19, v19, v19
	v_mul_f32_e32 v20, v8, v16
	v_mul_f32_e32 v24, v9, v16
	v_mul_f32_e32 v21, v8, v17
	v_mul_f32_e32 v25, v9, v17
	v_mul_f32_e32 v22, v8, v18
	v_mul_f32_e32 v26, v9, v18
	v_mul_f32_e32 v23, v8, v19
	v_mul_f32_e32 v27, v9, v19
	v_exp_f32_e32 v20, v20
	v_exp_f32_e32 v21, v21
	v_exp_f32_e32 v22, v22
	v_exp_f32_e32 v23, v23
	v_exp_f32_e32 v24, v24
	v_exp_f32_e32 v25, v25
	v_exp_f32_e32 v26, v26
	v_exp_f32_e32 v27, v27
	v_cvt_pk_f16_f32 v52, v20, v21
	v_cvt_pk_f16_f32 v53, v22, v23
	v_cvt_pk_f16_f32 v84, v24, v25
	v_cvt_pk_f16_f32 v85, v26, v27
	v_add_f32_e32 v16, 0x42a80000, v12
	v_add_f32_e32 v17, 0x42aa0000, v12
	v_add_f32_e32 v18, 0x42ac0000, v12
	v_add_f32_e32 v19, 0x42ae0000, v12
	v_mul_f32_e32 v16, v16, v16
	v_mul_f32_e32 v17, v17, v17
	v_mul_f32_e32 v18, v18, v18
	v_mul_f32_e32 v19, v19, v19
	v_mul_f32_e32 v20, v8, v16
	v_mul_f32_e32 v24, v9, v16
	v_mul_f32_e32 v21, v8, v17
	v_mul_f32_e32 v25, v9, v17
	v_mul_f32_e32 v22, v8, v18
	v_mul_f32_e32 v26, v9, v18
	v_mul_f32_e32 v23, v8, v19
	v_mul_f32_e32 v27, v9, v19
	v_exp_f32_e32 v20, v20
	v_exp_f32_e32 v21, v21
	v_exp_f32_e32 v22, v22
	v_exp_f32_e32 v23, v23
	v_exp_f32_e32 v24, v24
	v_exp_f32_e32 v25, v25
	v_exp_f32_e32 v26, v26
	v_exp_f32_e32 v27, v27
	v_cvt_pk_f16_f32 v54, v20, v21
	v_cvt_pk_f16_f32 v55, v22, v23
	v_cvt_pk_f16_f32 v86, v24, v25
	v_cvt_pk_f16_f32 v87, v26, v27
	v_add_f32_e32 v16, 0x42c00000, v12
	v_add_f32_e32 v17, 0x42c20000, v12
	v_add_f32_e32 v18, 0x42c40000, v12
	v_add_f32_e32 v19, 0x42c60000, v12
	v_mul_f32_e32 v16, v16, v16
	v_mul_f32_e32 v17, v17, v17
	v_mul_f32_e32 v18, v18, v18
	v_mul_f32_e32 v19, v19, v19
	v_mul_f32_e32 v20, v8, v16
	v_mul_f32_e32 v24, v9, v16
	v_mul_f32_e32 v21, v8, v17
	v_mul_f32_e32 v25, v9, v17
	v_mul_f32_e32 v22, v8, v18
	v_mul_f32_e32 v26, v9, v18
	v_mul_f32_e32 v23, v8, v19
	v_mul_f32_e32 v27, v9, v19
	v_exp_f32_e32 v20, v20
	v_exp_f32_e32 v21, v21
	v_exp_f32_e32 v22, v22
	v_exp_f32_e32 v23, v23
	v_exp_f32_e32 v24, v24
	v_exp_f32_e32 v25, v25
	v_exp_f32_e32 v26, v26
	v_exp_f32_e32 v27, v27
	v_cvt_pk_f16_f32 v56, v20, v21
	v_cvt_pk_f16_f32 v57, v22, v23
	v_cvt_pk_f16_f32 v88, v24, v25
	v_cvt_pk_f16_f32 v89, v26, v27
	v_add_f32_e32 v16, 0x42c80000, v12
	v_add_f32_e32 v17, 0x42ca0000, v12
	v_add_f32_e32 v18, 0x42cc0000, v12
	v_add_f32_e32 v19, 0x42ce0000, v12
	v_mul_f32_e32 v16, v16, v16
	v_mul_f32_e32 v17, v17, v17
	v_mul_f32_e32 v18, v18, v18
	v_mul_f32_e32 v19, v19, v19
	v_mul_f32_e32 v20, v8, v16
	v_mul_f32_e32 v24, v9, v16
	v_mul_f32_e32 v21, v8, v17
	v_mul_f32_e32 v25, v9, v17
	v_mul_f32_e32 v22, v8, v18
	v_mul_f32_e32 v26, v9, v18
	v_mul_f32_e32 v23, v8, v19
	v_mul_f32_e32 v27, v9, v19
	v_exp_f32_e32 v20, v20
	v_exp_f32_e32 v21, v21
	v_exp_f32_e32 v22, v22
	v_exp_f32_e32 v23, v23
	v_exp_f32_e32 v24, v24
	v_exp_f32_e32 v25, v25
	v_exp_f32_e32 v26, v26
	v_exp_f32_e32 v27, v27
	v_cvt_pk_f16_f32 v58, v20, v21
	v_cvt_pk_f16_f32 v59, v22, v23
	v_cvt_pk_f16_f32 v90, v24, v25
	v_cvt_pk_f16_f32 v91, v26, v27
	v_add_f32_e32 v16, 0x42e00000, v12
	v_add_f32_e32 v17, 0x42e20000, v12
	v_add_f32_e32 v18, 0x42e40000, v12
	v_add_f32_e32 v19, 0x42e60000, v12
	v_mul_f32_e32 v16, v16, v16
	v_mul_f32_e32 v17, v17, v17
	v_mul_f32_e32 v18, v18, v18
	v_mul_f32_e32 v19, v19, v19
	v_mul_f32_e32 v20, v8, v16
	v_mul_f32_e32 v24, v9, v16
	v_mul_f32_e32 v21, v8, v17
	v_mul_f32_e32 v25, v9, v17
	v_mul_f32_e32 v22, v8, v18
	v_mul_f32_e32 v26, v9, v18
	v_mul_f32_e32 v23, v8, v19
	v_mul_f32_e32 v27, v9, v19
	v_exp_f32_e32 v20, v20
	v_exp_f32_e32 v21, v21
	v_exp_f32_e32 v22, v22
	v_exp_f32_e32 v23, v23
	v_exp_f32_e32 v24, v24
	v_exp_f32_e32 v25, v25
	v_exp_f32_e32 v26, v26
	v_exp_f32_e32 v27, v27
	v_cvt_pk_f16_f32 v60, v20, v21
	v_cvt_pk_f16_f32 v61, v22, v23
	v_cvt_pk_f16_f32 v92, v24, v25
	v_cvt_pk_f16_f32 v93, v26, v27
	v_add_f32_e32 v16, 0x42e80000, v12
	v_add_f32_e32 v17, 0x42ea0000, v12
	v_add_f32_e32 v18, 0x42ec0000, v12
	v_add_f32_e32 v19, 0x42ee0000, v12
	v_mul_f32_e32 v16, v16, v16
	v_mul_f32_e32 v17, v17, v17
	v_mul_f32_e32 v18, v18, v18
	v_mul_f32_e32 v19, v19, v19
	v_mul_f32_e32 v20, v8, v16
	v_mul_f32_e32 v24, v9, v16
	v_mul_f32_e32 v21, v8, v17
	v_mul_f32_e32 v25, v9, v17
	v_mul_f32_e32 v22, v8, v18
	v_mul_f32_e32 v26, v9, v18
	v_mul_f32_e32 v23, v8, v19
	v_mul_f32_e32 v27, v9, v19
	v_exp_f32_e32 v20, v20
	v_exp_f32_e32 v21, v21
	v_exp_f32_e32 v22, v22
	v_exp_f32_e32 v23, v23
	v_exp_f32_e32 v24, v24
	v_exp_f32_e32 v25, v25
	v_exp_f32_e32 v26, v26
	v_exp_f32_e32 v27, v27
	v_cvt_pk_f16_f32 v62, v20, v21
	v_cvt_pk_f16_f32 v63, v22, v23
	v_cvt_pk_f16_f32 v94, v24, v25
	v_cvt_pk_f16_f32 v95, v26, v27
	v_mul_f32_e32 v16, v13, v13
	v_add_f32_e32 v17, 0x3f800000, v13
	v_add_f32_e32 v18, 0x40000000, v13
	v_add_f32_e32 v19, 0x40400000, v13
	v_mul_f32_e32 v17, v17, v17
	v_mul_f32_e32 v18, v18, v18
	v_mul_f32_e32 v19, v19, v19
	v_mul_f32_e32 v20, v8, v16
	v_mul_f32_e32 v24, v9, v16
	v_mul_f32_e32 v21, v8, v17
	v_mul_f32_e32 v25, v9, v17
	v_mul_f32_e32 v22, v8, v18
	v_mul_f32_e32 v26, v9, v18
	v_mul_f32_e32 v23, v8, v19
	v_mul_f32_e32 v27, v9, v19
	v_exp_f32_e32 v20, v20
	v_exp_f32_e32 v21, v21
	v_exp_f32_e32 v22, v22
	v_exp_f32_e32 v23, v23
	v_exp_f32_e32 v24, v24
	v_exp_f32_e32 v25, v25
	v_exp_f32_e32 v26, v26
	v_exp_f32_e32 v27, v27
	v_mul_f32_e32 v96, v10, v20
	v_mul_f32_e32 v97, v10, v21
	v_mul_f32_e32 v98, v10, v22
	v_mul_f32_e32 v99, v10, v23
	v_mul_f32_e32 v112, v11, v24
	v_mul_f32_e32 v113, v11, v25
	v_mul_f32_e32 v114, v11, v26
	v_mul_f32_e32 v115, v11, v27
	v_add_f32_e32 v16, 0x41000000, v13
	v_add_f32_e32 v17, 0x41100000, v13
	v_add_f32_e32 v18, 0x41200000, v13
	v_add_f32_e32 v19, 0x41300000, v13
	v_mul_f32_e32 v16, v16, v16
	v_mul_f32_e32 v17, v17, v17
	v_mul_f32_e32 v18, v18, v18
	v_mul_f32_e32 v19, v19, v19
	v_mul_f32_e32 v20, v8, v16
	v_mul_f32_e32 v24, v9, v16
	v_mul_f32_e32 v21, v8, v17
	v_mul_f32_e32 v25, v9, v17
	v_mul_f32_e32 v22, v8, v18
	v_mul_f32_e32 v26, v9, v18
	v_mul_f32_e32 v23, v8, v19
	v_mul_f32_e32 v27, v9, v19
	v_exp_f32_e32 v20, v20
	v_exp_f32_e32 v21, v21
	v_exp_f32_e32 v22, v22
	v_exp_f32_e32 v23, v23
	v_exp_f32_e32 v24, v24
	v_exp_f32_e32 v25, v25
	v_exp_f32_e32 v26, v26
	v_exp_f32_e32 v27, v27
	v_mul_f32_e32 v100, v10, v20
	v_mul_f32_e32 v101, v10, v21
	v_mul_f32_e32 v102, v10, v22
	v_mul_f32_e32 v103, v10, v23
	v_mul_f32_e32 v116, v11, v24
	v_mul_f32_e32 v117, v11, v25
	v_mul_f32_e32 v118, v11, v26
	v_mul_f32_e32 v119, v11, v27
	v_add_f32_e32 v16, 0x41800000, v13
	v_add_f32_e32 v17, 0x41880000, v13
	v_add_f32_e32 v18, 0x41900000, v13
	v_add_f32_e32 v19, 0x41980000, v13
	v_mul_f32_e32 v16, v16, v16
	v_mul_f32_e32 v17, v17, v17
	v_mul_f32_e32 v18, v18, v18
	v_mul_f32_e32 v19, v19, v19
	v_mul_f32_e32 v20, v8, v16
	v_mul_f32_e32 v24, v9, v16
	v_mul_f32_e32 v21, v8, v17
	v_mul_f32_e32 v25, v9, v17
	v_mul_f32_e32 v22, v8, v18
	v_mul_f32_e32 v26, v9, v18
	v_mul_f32_e32 v23, v8, v19
	v_mul_f32_e32 v27, v9, v19
	v_exp_f32_e32 v20, v20
	v_exp_f32_e32 v21, v21
	v_exp_f32_e32 v22, v22
	v_exp_f32_e32 v23, v23
	v_exp_f32_e32 v24, v24
	v_exp_f32_e32 v25, v25
	v_exp_f32_e32 v26, v26
	v_exp_f32_e32 v27, v27
	v_mul_f32_e32 v104, v10, v20
	v_mul_f32_e32 v105, v10, v21
	v_mul_f32_e32 v106, v10, v22
	v_mul_f32_e32 v107, v10, v23
	v_mul_f32_e32 v120, v11, v24
	v_mul_f32_e32 v121, v11, v25
	v_mul_f32_e32 v122, v11, v26
	v_mul_f32_e32 v123, v11, v27
	v_add_f32_e32 v16, 0x41c00000, v13
	v_add_f32_e32 v17, 0x41c80000, v13
	v_add_f32_e32 v18, 0x41d00000, v13
	v_add_f32_e32 v19, 0x41d80000, v13
	v_mul_f32_e32 v16, v16, v16
	v_mul_f32_e32 v17, v17, v17
	v_mul_f32_e32 v18, v18, v18
	v_mul_f32_e32 v19, v19, v19
	v_mul_f32_e32 v20, v8, v16
	v_mul_f32_e32 v24, v9, v16
	v_mul_f32_e32 v21, v8, v17
	v_mul_f32_e32 v25, v9, v17
	v_mul_f32_e32 v22, v8, v18
	v_mul_f32_e32 v26, v9, v18
	v_mul_f32_e32 v23, v8, v19
	v_mul_f32_e32 v27, v9, v19
	v_exp_f32_e32 v20, v20
	v_exp_f32_e32 v21, v21
	v_exp_f32_e32 v22, v22
	v_exp_f32_e32 v23, v23
	v_exp_f32_e32 v24, v24
	v_exp_f32_e32 v25, v25
	v_exp_f32_e32 v26, v26
	v_exp_f32_e32 v27, v27
	v_mul_f32_e32 v108, v10, v20
	v_mul_f32_e32 v109, v10, v21
	v_mul_f32_e32 v110, v10, v22
	v_mul_f32_e32 v111, v10, v23
	v_mul_f32_e32 v124, v11, v24
	v_mul_f32_e32 v125, v11, v25
	v_mul_f32_e32 v126, v11, v26
	v_mul_f32_e32 v127, v11, v27
	s_cmp_ge_u32 s28, 4
	s_cbranch_scc1 .Lloads
.Lconsume:
	s_waitcnt vmcnt(28)
	v_add_f32_e32 v128, v128, v129
	v_add_f32_e32 v130, v130, v131
	v_add_f32_e32 v132, v132, v133
	v_add_f32_e32 v134, v134, v135
	v_add_f32_e32 v136, v136, v137
	v_add_f32_e32 v138, v138, v139
	v_add_f32_e32 v140, v140, v141
	v_add_f32_e32 v142, v142, v143
	v_add_f32_e32 v128, v128, v130
	v_add_f32_e32 v132, v132, v134
	v_add_f32_e32 v136, v136, v138
	v_add_f32_e32 v140, v140, v142
	v_cndmask_b32_e64 v130, v128, v132, s[30:31]
	v_cndmask_b32_e64 v134, v136, v140, s[30:31]
	v_cndmask_b32_e64 v129, v132, v128, s[30:31]
	v_cndmask_b32_e64 v133, v140, v136, s[30:31]
	v_add_f32_dpp v129, v130, v129 quad_perm:[1,0,3,2] row_mask:0xf bank_mask:0xf bound_ctrl:1
	v_add_f32_dpp v133, v134, v133 quad_perm:[1,0,3,2] row_mask:0xf bank_mask:0xf bound_ctrl:1
	v_cndmask_b32_e64 v135, v129, v133, s[32:33]
	v_cndmask_b32_e64 v131, v133, v129, s[32:33]
	s_nop 1
	v_add_f32_dpp v131, v135, v131 quad_perm:[2,3,0,1] row_mask:0xf bank_mask:0xf bound_ctrl:1
	v_cvt_f16_f32_e32 v131, v131
	ds_write_b16 v14, v131 offset:0
	s_waitcnt vmcnt(24)
	v_add_f32_e32 v144, v144, v145
	v_add_f32_e32 v146, v146, v147
	v_add_f32_e32 v148, v148, v149
	v_add_f32_e32 v150, v150, v151
	v_add_f32_e32 v152, v152, v153
	v_add_f32_e32 v154, v154, v155
	v_add_f32_e32 v156, v156, v157
	v_add_f32_e32 v158, v158, v159
	v_add_f32_e32 v144, v144, v146
	v_add_f32_e32 v148, v148, v150
	v_add_f32_e32 v152, v152, v154
	v_add_f32_e32 v156, v156, v158
	v_cndmask_b32_e64 v146, v144, v148, s[30:31]
	v_cndmask_b32_e64 v150, v152, v156, s[30:31]
	v_cndmask_b32_e64 v145, v148, v144, s[30:31]
	v_cndmask_b32_e64 v149, v156, v152, s[30:31]
	v_add_f32_dpp v145, v146, v145 quad_perm:[1,0,3,2] row_mask:0xf bank_mask:0xf bound_ctrl:1
	v_add_f32_dpp v149, v150, v149 quad_perm:[1,0,3,2] row_mask:0xf bank_mask:0xf bound_ctrl:1
	v_cndmask_b32_e64 v151, v145, v149, s[32:33]
	v_cndmask_b32_e64 v147, v149, v145, s[32:33]
	s_nop 1
	v_add_f32_dpp v147, v151, v147 quad_perm:[2,3,0,1] row_mask:0xf bank_mask:0xf bound_ctrl:1
	v_cvt_f16_f32_e32 v147, v147
	ds_write_b16 v14, v147 offset:1088
	s_waitcnt vmcnt(20)
	v_add_f32_e32 v160, v160, v161
	v_add_f32_e32 v162, v162, v163
	v_add_f32_e32 v164, v164, v165
	v_add_f32_e32 v166, v166, v167
	v_add_f32_e32 v168, v168, v169
	v_add_f32_e32 v170, v170, v171
	v_add_f32_e32 v172, v172, v173
	v_add_f32_e32 v174, v174, v175
	v_add_f32_e32 v160, v160, v162
	v_add_f32_e32 v164, v164, v166
	v_add_f32_e32 v168, v168, v170
	v_add_f32_e32 v172, v172, v174
	v_cndmask_b32_e64 v162, v160, v164, s[30:31]
	v_cndmask_b32_e64 v166, v168, v172, s[30:31]
	v_cndmask_b32_e64 v161, v164, v160, s[30:31]
	v_cndmask_b32_e64 v165, v172, v168, s[30:31]
	v_add_f32_dpp v161, v162, v161 quad_perm:[1,0,3,2] row_mask:0xf bank_mask:0xf bound_ctrl:1
	v_add_f32_dpp v165, v166, v165 quad_perm:[1,0,3,2] row_mask:0xf bank_mask:0xf bound_ctrl:1
	v_cndmask_b32_e64 v167, v161, v165, s[32:33]
	v_cndmask_b32_e64 v163, v165, v161, s[32:33]
	s_nop 1
	v_add_f32_dpp v163, v167, v163 quad_perm:[2,3,0,1] row_mask:0xf bank_mask:0xf bound_ctrl:1
	v_cvt_f16_f32_e32 v163, v163
	ds_write_b16 v14, v163 offset:2176
	s_waitcnt vmcnt(16)
	v_add_f32_e32 v176, v176, v177
	v_add_f32_e32 v178, v178, v179
	v_add_f32_e32 v180, v180, v181
	v_add_f32_e32 v182, v182, v183
	v_add_f32_e32 v184, v184, v185
	v_add_f32_e32 v186, v186, v187
	v_add_f32_e32 v188, v188, v189
	v_add_f32_e32 v190, v190, v191
	v_add_f32_e32 v176, v176, v178
	v_add_f32_e32 v180, v180, v182
	v_add_f32_e32 v184, v184, v186
	v_add_f32_e32 v188, v188, v190
	v_cndmask_b32_e64 v178, v176, v180, s[30:31]
	v_cndmask_b32_e64 v182, v184, v188, s[30:31]
	v_cndmask_b32_e64 v177, v180, v176, s[30:31]
	v_cndmask_b32_e64 v181, v188, v184, s[30:31]
	v_add_f32_dpp v177, v178, v177 quad_perm:[1,0,3,2] row_mask:0xf bank_mask:0xf bound_ctrl:1
	v_add_f32_dpp v181, v182, v181 quad_perm:[1,0,3,2] row_mask:0xf bank_mask:0xf bound_ctrl:1
	v_cndmask_b32_e64 v183, v177, v181, s[32:33]
	v_cndmask_b32_e64 v179, v181, v177, s[32:33]
	s_nop 1
	v_add_f32_dpp v179, v183, v179 quad_perm:[2,3,0,1] row_mask:0xf bank_mask:0xf bound_ctrl:1
	v_cvt_f16_f32_e32 v179, v179
	ds_write_b16 v14, v179 offset:3264
	s_waitcnt vmcnt(12)
	v_add_f32_e32 v192, v192, v193
	v_add_f32_e32 v194, v194, v195
	v_add_f32_e32 v196, v196, v197
	v_add_f32_e32 v198, v198, v199
	v_add_f32_e32 v200, v200, v201
	v_add_f32_e32 v202, v202, v203
	v_add_f32_e32 v204, v204, v205
	v_add_f32_e32 v206, v206, v207
	v_add_f32_e32 v192, v192, v194
	v_add_f32_e32 v196, v196, v198
	v_add_f32_e32 v200, v200, v202
	v_add_f32_e32 v204, v204, v206
	v_cndmask_b32_e64 v194, v192, v196, s[30:31]
	v_cndmask_b32_e64 v198, v200, v204, s[30:31]
	v_cndmask_b32_e64 v193, v196, v192, s[30:31]
	v_cndmask_b32_e64 v197, v204, v200, s[30:31]
	v_add_f32_dpp v193, v194, v193 quad_perm:[1,0,3,2] row_mask:0xf bank_mask:0xf bound_ctrl:1
	v_add_f32_dpp v197, v198, v197 quad_perm:[1,0,3,2] row_mask:0xf bank_mask:0xf bound_ctrl:1
	v_cndmask_b32_e64 v199, v193, v197, s[32:33]
	v_cndmask_b32_e64 v195, v197, v193, s[32:33]
	s_nop 1
	v_add_f32_dpp v195, v199, v195 quad_perm:[2,3,0,1] row_mask:0xf bank_mask:0xf bound_ctrl:1
	v_cvt_f16_f32_e32 v195, v195
	ds_write_b16 v14, v195 offset:4352
	s_waitcnt vmcnt(8)
	v_add_f32_e32 v208, v208, v209
	v_add_f32_e32 v210, v210, v211
	v_add_f32_e32 v212, v212, v213
	v_add_f32_e32 v214, v214, v215
	v_add_f32_e32 v216, v216, v217
	v_add_f32_e32 v218, v218, v219
	v_add_f32_e32 v220, v220, v221
	v_add_f32_e32 v222, v222, v223
	v_add_f32_e32 v208, v208, v210
	v_add_f32_e32 v212, v212, v214
	v_add_f32_e32 v216, v216, v218
	v_add_f32_e32 v220, v220, v222
	v_cndmask_b32_e64 v210, v208, v212, s[30:31]
	v_cndmask_b32_e64 v214, v216, v220, s[30:31]
	v_cndmask_b32_e64 v209, v212, v208, s[30:31]
	v_cndmask_b32_e64 v213, v220, v216, s[30:31]
	v_add_f32_dpp v209, v210, v209 quad_perm:[1,0,3,2] row_mask:0xf bank_mask:0xf bound_ctrl:1
	v_add_f32_dpp v213, v214, v213 quad_perm:[1,0,3,2] row_mask:0xf bank_mask:0xf bound_ctrl:1
	v_cndmask_b32_e64 v215, v209, v213, s[32:33]
	v_cndmask_b32_e64 v211, v213, v209, s[32:33]
	s_nop 1
	v_add_f32_dpp v211, v215, v211 quad_perm:[2,3,0,1] row_mask:0xf bank_mask:0xf bound_ctrl:1
	v_cvt_f16_f32_e32 v211, v211
	ds_write_b16 v14, v211 offset:5440
	s_waitcnt vmcnt(4)
	v_add_f32_e32 v224, v224, v225
	v_add_f32_e32 v226, v226, v227
	v_add_f32_e32 v228, v228, v229
	v_add_f32_e32 v230, v230, v231
	v_add_f32_e32 v232, v232, v233
	v_add_f32_e32 v234, v234, v235
	v_add_f32_e32 v236, v236, v237
	v_add_f32_e32 v238, v238, v239
	v_add_f32_e32 v224, v224, v226
	v_add_f32_e32 v228, v228, v230
	v_add_f32_e32 v232, v232, v234
	v_add_f32_e32 v236, v236, v238
	v_cndmask_b32_e64 v226, v224, v228, s[30:31]
	v_cndmask_b32_e64 v230, v232, v236, s[30:31]
	v_cndmask_b32_e64 v225, v228, v224, s[30:31]
	v_cndmask_b32_e64 v229, v236, v232, s[30:31]
	v_add_f32_dpp v225, v226, v225 quad_perm:[1,0,3,2] row_mask:0xf bank_mask:0xf bound_ctrl:1
	v_add_f32_dpp v229, v230, v229 quad_perm:[1,0,3,2] row_mask:0xf bank_mask:0xf bound_ctrl:1
	v_cndmask_b32_e64 v231, v225, v229, s[32:33]
	v_cndmask_b32_e64 v227, v229, v225, s[32:33]
	s_nop 1
	v_add_f32_dpp v227, v231, v227 quad_perm:[2,3,0,1] row_mask:0xf bank_mask:0xf bound_ctrl:1
	v_cvt_f16_f32_e32 v227, v227
	ds_write_b16 v14, v227 offset:6528
	s_waitcnt vmcnt(0)
	v_add_f32_e32 v240, v240, v241
	v_add_f32_e32 v242, v242, v243
	v_add_f32_e32 v244, v244, v245
	v_add_f32_e32 v246, v246, v247
	v_add_f32_e32 v248, v248, v249
	v_add_f32_e32 v250, v250, v251
	v_add_f32_e32 v252, v252, v253
	v_add_f32_e32 v254, v254, v255
	v_add_f32_e32 v240, v240, v242
	v_add_f32_e32 v244, v244, v246
	v_add_f32_e32 v248, v248, v250
	v_add_f32_e32 v252, v252, v254
	v_cndmask_b32_e64 v242, v240, v244, s[30:31]
	v_cndmask_b32_e64 v246, v248, v252, s[30:31]
	v_cndmask_b32_e64 v241, v244, v240, s[30:31]
	v_cndmask_b32_e64 v245, v252, v248, s[30:31]
	v_add_f32_dpp v241, v242, v241 quad_perm:[1,0,3,2] row_mask:0xf bank_mask:0xf bound_ctrl:1
	v_add_f32_dpp v245, v246, v245 quad_perm:[1,0,3,2] row_mask:0xf bank_mask:0xf bound_ctrl:1
	v_cndmask_b32_e64 v247, v241, v245, s[32:33]
	v_cndmask_b32_e64 v243, v245, v241, s[32:33]
	s_nop 1
	v_add_f32_dpp v243, v247, v243 quad_perm:[2,3,0,1] row_mask:0xf bank_mask:0xf bound_ctrl:1
	v_cvt_f16_f32_e32 v243, v243
	ds_write_b16 v14, v243 offset:7616
	s_waitcnt lgkmcnt(0)
	s_barrier
	ds_read_b128 v[160:163], v15 offset:0
	ds_read_b128 v[164:167], v15 offset:32
	ds_read_b128 v[168:171], v15 offset:64
	ds_read_b128 v[172:175], v15 offset:96
	ds_read_b128 v[176:179], v15 offset:128
	ds_read_b128 v[180:183], v15 offset:160
	ds_read_b128 v[184:187], v15 offset:192
	ds_read_b128 v[188:191], v15 offset:224
	s_waitcnt lgkmcnt(7)
	v_mfma_f32_32x32x16_f16 v[128:143], v[160:163], v[32:35], 0
	v_mfma_f32_32x32x16_f16 v[144:159], v[160:163], v[64:67], 0
	s_waitcnt lgkmcnt(6)
	v_mfma_f32_32x32x16_f16 v[128:143], v[164:167], v[36:39], v[128:143]
	v_mfma_f32_32x32x16_f16 v[144:159], v[164:167], v[68:71], v[144:159]
	s_waitcnt lgkmcnt(5)
	v_mfma_f32_32x32x16_f16 v[128:143], v[168:171], v[40:43], v[128:143]
	v_mfma_f32_32x32x16_f16 v[144:159], v[168:171], v[72:75], v[144:159]
	s_waitcnt lgkmcnt(4)
	v_mfma_f32_32x32x16_f16 v[128:143], v[172:175], v[44:47], v[128:143]
	v_mfma_f32_32x32x16_f16 v[144:159], v[172:175], v[76:79], v[144:159]
	s_waitcnt lgkmcnt(3)
	v_mfma_f32_32x32x16_f16 v[128:143], v[176:179], v[48:51], v[128:143]
	v_mfma_f32_32x32x16_f16 v[144:159], v[176:179], v[80:83], v[144:159]
	s_waitcnt lgkmcnt(2)
	v_mfma_f32_32x32x16_f16 v[128:143], v[180:183], v[52:55], v[128:143]
	v_mfma_f32_32x32x16_f16 v[144:159], v[180:183], v[84:87], v[144:159]
	s_waitcnt lgkmcnt(1)
	v_mfma_f32_32x32x16_f16 v[128:143], v[184:187], v[56:59], v[128:143]
	v_mfma_f32_32x32x16_f16 v[144:159], v[184:187], v[88:91], v[144:159]
	s_waitcnt lgkmcnt(0)
	v_mfma_f32_32x32x16_f16 v[128:143], v[188:191], v[60:63], v[128:143]
	v_mfma_f32_32x32x16_f16 v[144:159], v[188:191], v[92:95], v[144:159]
	s_nop 15
	s_nop 3
	v_mul_f32_e32 v16, v96, v128
	v_mul_f32_e32 v17, v97, v129
	v_mul_f32_e32 v18, v98, v130
	v_mul_f32_e32 v19, v99, v131
	v_fma_f32 v16, -v112, v144, v16
	v_fma_f32 v17, -v113, v145, v17
	v_fma_f32 v18, -v114, v146, v18
	v_fma_f32 v19, -v115, v147, v19
	v_fma_f32 v16, v100, v132, v16
	v_fma_f32 v16, -v116, v148, v16
	v_fma_f32 v17, v101, v133, v17
	v_fma_f32 v17, -v117, v149, v17
	v_fma_f32 v18, v102, v134, v18
	v_fma_f32 v18, -v118, v150, v18
	v_fma_f32 v19, v103, v135, v19
	v_fma_f32 v19, -v119, v151, v19
	v_fma_f32 v16, v104, v136, v16
	v_fma_f32 v16, -v120, v152, v16
	v_fma_f32 v17, v105, v137, v17
	v_fma_f32 v17, -v121, v153, v17
	v_fma_f32 v18, v106, v138, v18
	v_fma_f32 v18, -v122, v154, v18
	v_fma_f32 v19, v107, v139, v19
	v_fma_f32 v19, -v123, v155, v19
	v_fma_f32 v16, v108, v140, v16
	v_fma_f32 v16, -v124, v156, v16
	v_fma_f32 v17, v109, v141, v17
	v_fma_f32 v17, -v125, v157, v17
	v_fma_f32 v18, v110, v142, v18
	v_fma_f32 v18, -v126, v158, v18
	v_fma_f32 v19, v111, v143, v19
	v_fma_f32 v19, -v127, v159, v19
	v_add_f32_e32 v16, v16, v17
	v_add_f32_e32 v18, v18, v19
	v_add_f32_e32 v16, v16, v18
	v_mov_b32_e32 v17, v16
	s_lshl_b32 s6, s6, 6
	s_add_i32 s6, s6, s7
	s_lshl_b32 s6, s6, 10
	v_permlane32_swap_b32_e32 v16, v17
	v_add_u32_e32 v5, s6, v5
	v_cmp_gt_u32_e32 vcc, 32, v1
	v_add_f32_e32 v16, v16, v17
	s_and_saveexec_b64 s[2:3], vcc
	s_cbranch_execz .Ldog_main_done
	global_store_dword v5, v16, s[26:27]
